# batch9: + P5 next-head prefetch issued at the head's top (behind the z loads) instead of behind the M build
# speedup vs baseline: 1.0050x; 1.0050x over previous
.LBB0_565:
	v_lshl_add_u64 v[128:129], s[92:93], 0, v[126:127]
	s_mov_b32 s4, 0x3dc00000
	v_add_co_u32_e32 v198, vcc, s4, v128
	v_readlane_b32 s6, v11, s2
	s_nop 0
	v_addc_co_u32_e32 v199, vcc, 0, v129, vcc
	v_mov_b64_e32 v[74:75], v[200:201]
	v_mov_b64_e32 v[76:77], v[202:203]
	v_mov_b64_e32 v[70:71], v[216:217]
	v_mov_b64_e32 v[72:73], v[218:219]
	global_load_dwordx4 v[200:203], v[198:199], off offset:128
	global_load_dwordx4 v[216:219], v[198:199], off offset:192
	s_cmpk_eq_i32 s0, 0x700
	s_cbranch_scc1 .Lp5_pf_skip
	v_lshl_add_u64 v[8:9], s[92:93], 0, v[118:119]
	v_add_co_u32_e32 v14, vcc, 0x45c00000, v8
	v_lshl_add_u64 v[2:3], s[92:93], 0, v[124:125]
	s_nop 0
	v_addc_co_u32_e32 v15, vcc, 0, v9, vcc
	v_add_co_u32_e32 v16, vcc, 0x45c03000, v8
	v_lshl_add_u64 v[4:5], s[92:93], 0, v[122:123]
	s_nop 0
	v_addc_co_u32_e32 v17, vcc, 0, v9, vcc
	v_add_co_u32_e32 v18, vcc, 0x45c06000, v8
	v_lshl_add_u64 v[6:7], s[92:93], 0, v[120:121]
	s_nop 0
	v_addc_co_u32_e32 v19, vcc, 0, v9, vcc
	v_add_co_u32_e32 v20, vcc, 0x45c09000, v8
	s_nop 1
	v_addc_co_u32_e32 v21, vcc, 0, v9, vcc
	v_add_co_u32_e32 v94, vcc, 0x45c0c000, v8
	s_nop 1
	v_addc_co_u32_e32 v95, vcc, 0, v9, vcc
	global_load_dword v2, v[2:3], off
	s_nop 0
	global_load_dword v1, v[4:5], off
	global_load_dword v12, v[6:7], off
	global_load_dword v3, v[14:15], off offset:128
	s_nop 0
	global_load_dword v4, v[16:17], off offset:128
	global_load_dword v5, v[18:19], off offset:128
	global_load_dword v6, v[20:21], off offset:128
	global_load_dword v7, v[94:95], off offset:128
	v_add_co_u32_e32 v14, vcc, 0x45c0f000, v8
	v_lshl_add_u64 v[18:19], s[92:93], 0, v[116:117]
	s_nop 0
	v_addc_co_u32_e32 v15, vcc, 0, v9, vcc
	v_add_co_u32_e32 v16, vcc, 0x45c12000, v8
	s_nop 1
	v_addc_co_u32_e32 v17, vcc, 0, v9, vcc
	global_load_dword v8, v[14:15], off offset:128
	global_load_dword v9, v[16:17], off offset:128
	global_load_dword v10, v[18:19], off
	v_lshl_add_u64 v[14:15], v[110:111], 0, s[0:1]
	v_add_co_u32_e32 v16, vcc, s12, v14
	s_nop 1
	v_addc_co_u32_e32 v17, vcc, 0, v15, vcc
	v_add_co_u32_e32 v18, vcc, s13, v14
	s_nop 1
	v_addc_co_u32_e32 v19, vcc, 0, v15, vcc
	v_add_co_u32_e32 v20, vcc, s48, v14
	s_nop 1
	v_addc_co_u32_e32 v21, vcc, 0, v15, vcc
	global_load_dwordx2 v[176:177], v[14:15], off offset:256
	global_load_dwordx2 v[178:179], v[16:17], off offset:256
	global_load_dwordx2 v[180:181], v[18:19], off offset:256
	global_load_dwordx2 v[182:183], v[20:21], off offset:256
	v_lshl_add_u64 v[14:15], v[112:113], 0, s[0:1]
	global_load_dwordx2 v[184:185], v[14:15], off
	v_lshl_add_u64 v[14:15], s[92:93], 0, v[114:115]
	v_add_co_u32_e32 v16, vcc, 0x5e004000, v14
	s_nop 1
	v_addc_co_u32_e32 v17, vcc, 0, v15, vcc
	v_add_co_u32_e32 v18, vcc, 0x5e006000, v14
	s_nop 1
	v_addc_co_u32_e32 v19, vcc, 0, v15, vcc
	global_load_dwordx4 v[14:17], v[16:17], off
	s_nop 0
	global_load_dwordx4 v[18:21], v[18:19], off
.Lp5_pf_skip:
	ds_read2st64_b32 v[130:131], v13 offset1:16
	s_and_b32 s52, s2, 1
	s_add_i32 s51, 0, 0xa800
	s_cmp_eq_u32 s52, 0
	s_cselect_b64 s[90:91], -1, 0
	s_waitcnt lgkmcnt(0)
	v_div_scale_f32 v102, s[4:5], v130, v130, s6
	v_rcp_f32_e32 v103, v102
	s_and_b64 s[4:5], s[90:91], exec
	s_cselect_b32 s4, s33, s51
	v_lshlrev_b32_e32 v143, 1, v164
	v_fma_f32 v78, -v102, v103, 1.0
	v_fmac_f32_e32 v103, v78, v103
	v_add3_u32 v78, s4, v222, v143
	v_add_u32_e32 v79, 0x1000, v78
	v_div_scale_f32 v104, vcc, s6, v130, s6
	ds_read_b128 v[94:97], v141
	ds_read_b128 v[98:101], v141 offset:64
	ds_read2_b64 v[90:93], v78 offset1:4
	ds_read2_b64 v[86:89], v79 offset0:32 offset1:36
	v_add_u32_e32 v79, 0x2000, v78
	v_add_u32_e32 v78, 0x3000, v78
	v_mul_f32_e32 v105, v104, v103
	ds_read2_b64 v[82:85], v79 offset0:64 offset1:68
	ds_read2_b64 v[78:81], v78 offset0:96 offset1:100
	v_fma_f32 v106, -v102, v105, v104
	v_fmac_f32_e32 v105, v106, v103
	v_fma_f32 v102, -v102, v105, v104
	v_div_fmas_f32 v132, v102, v103, v105
	s_waitcnt lgkmcnt(5)
	v_sub_f32_e32 v109, v131, v94
	s_mov_b64 s[4:5], -1
	s_and_b64 vcc, exec, s[82:83]
	s_waitcnt lgkmcnt(4)
	v_sub_f32_e32 v107, v131, v98
	v_sub_f32_e32 v108, v131, v95
	v_sub_f32_e32 v106, v131, v99
	v_sub_f32_e32 v105, v131, v96
	v_sub_f32_e32 v104, v131, v100
	v_sub_f32_e32 v103, v131, v97
	v_sub_f32_e32 v102, v131, v101
	s_cbranch_vccnz .LBB0_567
	v_mul_f32_e32 v95, 0x3fb8aa3b, v107
	v_mul_f32_e32 v99, 0x3fb8aa3b, v104
	v_mul_f32_e32 v94, 0x3fb8aa3b, v109
	v_exp_f32_e32 v96, v95
	v_mul_f32_e32 v95, 0x3fb8aa3b, v108
	v_mul_f32_e32 v97, 0x3fb8aa3b, v106
	v_mul_f32_e32 v98, 0x3fb8aa3b, v105
	v_exp_f32_e32 v100, v99
	v_mul_f32_e32 v99, 0x3fb8aa3b, v103
	v_mul_f32_e32 v101, 0x3fb8aa3b, v102
	v_exp_f32_e32 v94, v94
	v_exp_f32_e32 v95, v95
	v_exp_f32_e32 v97, v97
	v_exp_f32_e32 v98, v98
	v_exp_f32_e32 v99, v99
	v_exp_f32_e32 v101, v101
	v_pk_mul_f32 v[94:95], v[38:39], v[94:95]
	v_pk_mul_f32 v[96:97], v[46:47], v[96:97]
	v_pk_mul_f32 v[98:99], v[40:41], v[98:99]
	v_pk_mul_f32 v[100:101], v[48:49], v[100:101]
	s_mov_b64 s[4:5], 0

.LBB0_573:
.LBB0_574:
	s_and_b64 s[6:7], s[90:91], exec
	s_mov_b32 s6, 0xec00
	s_cselect_b32 s6, 0x17400, s6
	s_add_i32 s6, s6, 0
	v_add3_u32 v130, s6, v162, v222
	ds_read_b128 v[94:97], v130
	ds_read_b128 v[98:101], v130 offset:64
	ds_read_b128 v[102:105], v130 offset:4352
	ds_read_b128 v[106:109], v130 offset:4416
	ds_read_b128 v[132:135], v130 offset:8704
	ds_read_b128 v[136:139], v130 offset:8768
	ds_read_b128 v[144:147], v130 offset:13056
	ds_read_b128 v[148:151], v130 offset:13120
	s_waitcnt lgkmcnt(7)
	v_mfma_f32_16x16x32_bf16 v[94:97], v[94:97], v[22:25], 0
	s_waitcnt lgkmcnt(5)
	v_mfma_f32_16x16x32_bf16 v[102:105], v[102:105], v[22:25], 0
	s_waitcnt lgkmcnt(3)
	v_mfma_f32_16x16x32_bf16 v[132:135], v[132:135], v[22:25], 0
	s_waitcnt lgkmcnt(1)
	v_mfma_f32_16x16x32_bf16 v[144:147], v[144:147], v[22:25], 0
	ds_read_b128 v[152:155], v130 offset:128
	ds_read_b128 v[186:189], v130 offset:4480
	ds_read_b128 v[190:193], v130 offset:8832
	ds_read_b128 v[194:197], v130 offset:13184
	v_mfma_f32_16x16x32_bf16 v[94:97], v[98:101], v[26:29], v[94:97]
	v_mfma_f32_16x16x32_bf16 v[98:101], v[106:109], v[26:29], v[102:105]
	s_waitcnt lgkmcnt(4)
	v_mfma_f32_16x16x32_bf16 v[106:109], v[148:151], v[26:29], v[144:147]
	v_mfma_f32_16x16x32_bf16 v[102:105], v[136:139], v[26:29], v[132:135]
	s_nop 2
	ds_read_b128 v[132:135], v130 offset:192
	ds_read_b128 v[136:139], v130 offset:4544
	ds_read_b128 v[144:147], v130 offset:8896
	ds_read_b128 v[148:151], v130 offset:13248
	s_waitcnt lgkmcnt(7)
	v_mfma_f32_16x16x32_bf16 v[94:97], v[152:155], v[30:33], v[94:97]
	s_waitcnt lgkmcnt(6)
	v_mfma_f32_16x16x32_bf16 v[98:101], v[186:189], v[30:33], v[98:101]
	s_waitcnt lgkmcnt(4)
	v_mfma_f32_16x16x32_bf16 v[106:109], v[194:197], v[30:33], v[106:109]
	v_mfma_f32_16x16x32_bf16 v[152:155], v[190:193], v[30:33], v[102:105]
	s_waitcnt lgkmcnt(3)
	v_mfma_f32_16x16x32_bf16 v[132:135], v[132:135], v[34:37], v[94:97]
	s_waitcnt lgkmcnt(2)
	v_mfma_f32_16x16x32_bf16 v[102:105], v[136:139], v[34:37], v[98:101]
	s_waitcnt lgkmcnt(1)
	v_mfma_f32_16x16x32_bf16 v[98:101], v[144:147], v[34:37], v[152:155]
	s_waitcnt lgkmcnt(0)
	v_mfma_f32_16x16x32_bf16 v[94:97], v[148:151], v[34:37], v[106:109]
	s_nop 2
	v_mul_f32_e32 v106, 0x3fb8aa3b, v131
	s_cmpk_eq_i32 s0, 0x700
	s_cbranch_scc1 .Lp5_zw_last
	s_waitcnt vmcnt(20)
	s_branch .Lp5_zw_done
